# P12: nt on the 8 read-once H-row loads so they do not displace the gathered YS rows
# speedup vs baseline: 1.0012x; 1.0012x over previous
; #define GAS __attribute__((address_space(1)))
; #define LAS __attribute__((address_space(3)))
; __global__ void __launch_bounds__(NTHR, 2) mk_fwd(Args args) {
;     ...
;         LAS float* s_lnw = (LAS float*)lds; LAS float* s_lnb = s_lnw + 2048;
;         *(LAS f32x4*)(s_lnw + 4 * tid) = *(const GAS f32x4*)(ln2_w + 4 * tid); *(LAS f32x4*)(s_lnb + 4 * tid) = *(const GAS f32x4*)(ln2_b + 4 * tid);
;         __syncthreads();
;         int nsl[4]; float ngt[4];
; #pragma unroll
;         for (int k = 0; k < 4; ++k) { nsl[k] = SLOT_OF[gw * 4 + k]; ngt[k] = GATE[gw * 4 + k]; }
; #pragma unroll 1
;         for (int m = gw; m < M; m += NGW) {
;             int sl[4]; float gt[4];
; #pragma unroll
;             for (int k = 0; k < 4; ++k) { sl[k] = nsl[k]; gt[k] = ngt[k]; }
;             { const int mn = m + NGW < M ? m + NGW : m;
; #pragma unroll
;               for (int k = 0; k < 4; ++k) { nsl[k] = SLOT_OF[mn * 4 + k]; ngt[k] = GATE[mn * 4 + k]; } }
;             f32x4 v[8]; float s = 0.f;
; #pragma unroll
;             for (int q = 0; q < 8; ++q) { const int c = 4 * lane + 256 * q; f32x4 f = (f32x4){0.f, 0.f, 0.f, 0.f};
; #pragma unroll
;                 for (int k = 0; k < 4; ++k) { const unsigned yv = *(const GAS unsigned*)(YS + (size_t)sl[k] * D + c); const f32x2n lo2 = __builtin_amdgcn_cvt_pk_f32_fp8(yv, false), hi2 = __builtin_amdgcn_cvt_pk_f32_fp8(yv, true); f += (gt[k] * (1.0f / pg8::YS_SCALE)) * (f32x4){lo2.x, lo2.y, hi2.x, hi2.y}; }
;                 { const v2u hw = *(const GAS v2u*)(H + (size_t)m * D + c); v[q] = ALPHA * (f32x4){bflo(hw.x), bfhi(hw.x), bflo(hw.y), bfhi(hw.y)} + f; } s += (v[q].x + v[q].y) + (v[q].z + v[q].w); }
.LBB0_1219:
	s_waitcnt vmcnt(0)
	v_ashrrev_i32_e32 v97, 31, v64
	v_mov_b32_e32 v96, v64
	v_ashrrev_i32_e32 v99, 31, v65
	v_mov_b32_e32 v98, v65
	v_ashrrev_i32_e32 v101, 31, v66
	v_mov_b32_e32 v100, v66
	v_ashrrev_i32_e32 v103, 31, v67
	v_mov_b32_e32 v102, v67
	v_lshlrev_b64 v[96:97], 11, v[96:97]
	v_lshlrev_b64 v[98:99], 11, v[98:99]
	v_lshlrev_b64 v[100:101], 11, v[100:101]
	v_lshlrev_b64 v[102:103], 11, v[102:103]
	v_lshl_add_u64 v[124:125], v[74:75], 0, v[96:97]
	v_lshl_add_u64 v[96:97], s[8:9], 0, v[96:97]
	v_mul_f32_e32 v94, 0x3d800000, v68
	v_mul_f32_e32 v92, 0x3d800000, v69
	v_mul_f32_e32 v64, 0x3d800000, v70
	v_mul_f32_e32 v68, 0x3d800000, v71
	global_load_dwordx2 v[66:67], v[90:91], off nt
	global_load_dwordx2 v[70:71], v[90:91], off offset:512 nt
	global_load_dwordx2 v[104:105], v[90:91], off offset:1024 nt
	global_load_dwordx2 v[108:109], v[90:91], off offset:1536 nt
	global_load_dwordx2 v[110:111], v[90:91], off offset:2048 nt
	global_load_dwordx2 v[112:113], v[90:91], off offset:2560 nt
	global_load_dwordx2 v[114:115], v[90:91], off offset:3072 nt
	global_load_dwordx2 v[116:117], v[90:91], off offset:3584 nt
	v_lshl_add_u64 v[126:127], v[74:75], 0, v[98:99]
	v_lshl_add_u64 v[128:129], v[74:75], 0, v[100:101]
	v_lshl_add_u64 v[130:131], v[74:75], 0, v[102:103]
	global_load_dword v65, v[124:125], off
	global_load_dword v69, v[126:127], off
	global_load_dword v172, v[128:129], off
	global_load_dword v173, v[130:131], off
	v_lshl_add_u64 v[124:125], v[96:97], 0, v[72:73]
	s_add_i32 s0, s30, s28
	global_load_dword v174, v[124:125], off
	s_cmpk_lt_i32 s0, 0x4000
	s_cselect_b64 s[2:3], -1, 0
	s_and_b64 s[16:17], s[2:3], exec
	s_cselect_b32 s1, s0, s30
	v_lshl_add_u64 v[98:99], s[8:9], 0, v[98:99]
	s_mov_b32 s30, s0
	s_lshl_b32 s0, s1, 2
	v_lshl_add_u64 v[100:101], s[8:9], 0, v[100:101]
	v_lshl_add_u64 v[102:103], s[8:9], 0, v[102:103]
	v_lshl_add_u64 v[126:127], v[98:99], 0, v[72:73]
	s_ashr_i32 s1, s0, 31
	v_lshl_add_u64 v[128:129], v[100:101], 0, v[72:73]
	v_lshl_add_u64 v[130:131], v[102:103], 0, v[72:73]
	v_lshl_add_u64 v[132:133], v[96:97], 0, v[76:77]
	v_lshl_add_u64 v[134:135], v[98:99], 0, v[76:77]
	v_lshl_add_u64 v[136:137], v[100:101], 0, v[76:77]
	v_lshl_add_u64 v[138:139], v[102:103], 0, v[76:77]
	v_lshl_add_u64 v[140:141], v[96:97], 0, v[78:79]
	v_lshl_add_u64 v[142:143], v[98:99], 0, v[78:79]
	v_lshl_add_u64 v[144:145], v[100:101], 0, v[78:79]
	v_lshl_add_u64 v[146:147], v[102:103], 0, v[78:79]
	v_lshl_add_u64 v[148:149], v[96:97], 0, v[80:81]
	v_lshl_add_u64 v[150:151], v[98:99], 0, v[80:81]
	v_lshl_add_u64 v[152:153], v[100:101], 0, v[80:81]
	v_lshl_add_u64 v[154:155], v[102:103], 0, v[80:81]
	v_lshl_add_u64 v[156:157], v[96:97], 0, v[82:83]
	v_lshl_add_u64 v[158:159], v[98:99], 0, v[82:83]
	v_lshl_add_u64 v[160:161], v[100:101], 0, v[82:83]
	v_lshl_add_u64 v[162:163], v[102:103], 0, v[82:83]
	v_lshl_add_u64 v[164:165], v[96:97], 0, v[84:85]
	v_lshl_add_u64 v[166:167], v[98:99], 0, v[84:85]
	v_lshl_add_u64 v[168:169], v[100:101], 0, v[84:85]
	v_lshl_add_u64 v[170:171], v[102:103], 0, v[84:85]
	v_lshl_add_u64 v[96:97], v[96:97], 0, v[86:87]
	v_lshl_add_u64 v[98:99], v[98:99], 0, v[86:87]
	v_lshl_add_u64 v[100:101], v[100:101], 0, v[86:87]
	v_lshl_add_u64 v[102:103], v[102:103], 0, v[86:87]
	global_load_dword v175, v[126:127], off
	global_load_dword v176, v[128:129], off
	global_load_dword v177, v[130:131], off
	global_load_dword v178, v[132:133], off
	global_load_dword v179, v[134:135], off
	global_load_dword v182, v[136:137], off
	global_load_dword v186, v[138:139], off
	global_load_dword v190, v[140:141], off
	global_load_dword v194, v[142:143], off
	global_load_dword v198, v[144:145], off
	global_load_dword v202, v[146:147], off
	global_load_dword v206, v[148:149], off
	global_load_dword v210, v[150:151], off
	global_load_dword v214, v[152:153], off
	global_load_dword v218, v[154:155], off
	global_load_dword v222, v[156:157], off
	global_load_dword v226, v[158:159], off
	global_load_dword v230, v[160:161], off
	global_load_dword v234, v[162:163], off
	global_load_dword v238, v[164:165], off
	global_load_dword v242, v[166:167], off
	global_load_dword v246, v[168:169], off
	global_load_dword v248, v[170:171], off
	global_load_dword v244, v[96:97], off
	global_load_dword v249, v[98:99], off
	global_load_dword v250, v[100:101], off
	global_load_dword v251, v[102:103], off
	s_lshl_b64 s[0:1], s[0:1], 2
	s_add_u32 s16, s4, s0
	s_addc_u32 s17, s5, s1
	global_load_dwordx4 v[96:99], v73, s[16:17]
	s_add_u32 s18, s66, s0
	s_addc_u32 s19, s67, s1
	global_load_dwordx4 v[100:103], v73, s[18:19]
	v_mov_b32_e32 v120, 0
	v_mov_b32_e32 v121, 0
	s_and_b64 s[0:1], s[2:3], exec
	v_mov_b32_e32 v122, 0
	v_mov_b32_e32 v123, 0
	v_add_co_u32_e32 v106, vcc, s14, v88
	v_lshl_add_u64 v[90:91], v[90:91], 0, s[10:11]
	s_nop 0
	v_addc_co_u32_e32 v107, vcc, -1, v89, vcc
	s_waitcnt vmcnt(41)
	v_lshlrev_b32_e32 v124, 16, v66
	v_and_b32_e32 v125, 0xffff0000, v66
	v_lshlrev_b32_e32 v126, 16, v67
	v_and_b32_e32 v127, 0xffff0000, v67
	s_waitcnt vmcnt(40)
	v_lshlrev_b32_e32 v128, 16, v70
	v_and_b32_e32 v129, 0xffff0000, v70
	v_lshlrev_b32_e32 v70, 16, v71
	v_and_b32_e32 v71, 0xffff0000, v71
	s_waitcnt vmcnt(33)
	v_cvt_pk_f32_fp8_e32 v[66:67], v65
	v_cvt_pk_f32_fp8_sdwa v[142:143], v65 src0_sel:WORD_1
	s_waitcnt vmcnt(32)
	v_cvt_pk_f32_fp8_e32 v[144:145], v69
	v_cvt_pk_f32_fp8_sdwa v[146:147], v69 src0_sel:WORD_1
	s_waitcnt vmcnt(31)
	v_cvt_pk_f32_fp8_e32 v[148:149], v172
	v_cvt_pk_f32_fp8_sdwa v[150:151], v172 src0_sel:WORD_1
	s_waitcnt vmcnt(29)
; #define GAS __attribute__((address_space(1)))
; __global__ void __launch_bounds__(NTHR, 2) mk_fwd(Args args) {
;     ...
;             { const int mn = m + NGW < M ? m + NGW : m;
; #pragma unroll
;               for (int k = 0; k < 4; ++k) { nsl[k] = SLOT_OF[mn * 4 + k]; ngt[k] = GATE[mn * 4 + k]; } }
;             f32x4 v[8]; float s = 0.f;
; #pragma unroll
;             for (int q = 0; q < 8; ++q) { const int c = 4 * lane + 256 * q; f32x4 f = (f32x4){0.f, 0.f, 0.f, 0.f};
; #pragma unroll
;                 for (int k = 0; k < 4; ++k) { const unsigned yv = *(const GAS unsigned*)(YS + (size_t)sl[k] * D + c); const f32x2n lo2 = __builtin_amdgcn_cvt_pk_f32_fp8(yv, false), hi2 = __builtin_amdgcn_cvt_pk_f32_fp8(yv, true); f += (gt[k] * (1.0f / pg8::YS_SCALE)) * (f32x4){lo2.x, lo2.y, hi2.x, hi2.y}; }
	v_cvt_pk_f32_fp8_e32 v[156:157], v174
	v_cvt_pk_f32_fp8_e32 v[152:153], v173
	v_cvt_pk_f32_fp8_sdwa v[154:155], v173 src0_sel:WORD_1
	v_cvt_pk_f32_fp8_sdwa v[158:159], v174 src0_sel:WORD_1
	v_pk_fma_f32 v[66:67], v[66:67], v[94:95], 0 op_sel_hi:[1,0,0]
	v_pk_fma_f32 v[142:143], v[142:143], v[94:95], 0 op_sel_hi:[1,0,0]
	v_pk_fma_f32 v[66:67], v[144:145], v[92:93], v[66:67] op_sel_hi:[1,0,1]
	v_pk_fma_f32 v[142:143], v[146:147], v[92:93], v[142:143] op_sel_hi:[1,0,1]
	v_pk_fma_f32 v[156:157], v[156:157], v[94:95], 0 op_sel_hi:[1,0,0]
	v_pk_fma_f32 v[158:159], v[158:159], v[94:95], 0 op_sel_hi:[1,0,0]
	v_pk_fma_f32 v[142:143], v[150:151], v[64:65], v[142:143] op_sel_hi:[1,0,1]
	v_pk_fma_f32 v[66:67], v[148:149], v[64:65], v[66:67] op_sel_hi:[1,0,1]
	s_waitcnt vmcnt(28)
	v_cvt_pk_f32_fp8_e32 v[160:161], v175
	v_cvt_pk_f32_fp8_sdwa v[162:163], v175 src0_sel:WORD_1
	s_waitcnt vmcnt(27)
	v_cvt_pk_f32_fp8_e32 v[164:165], v176
	s_waitcnt vmcnt(25)
	v_cvt_pk_f32_fp8_e32 v[172:173], v178
	v_cvt_pk_f32_fp8_sdwa v[166:167], v176 src0_sel:WORD_1
	v_cvt_pk_f32_fp8_e32 v[168:169], v177
	v_cvt_pk_f32_fp8_sdwa v[170:171], v177 src0_sel:WORD_1
	s_waitcnt vmcnt(24)
	v_cvt_pk_f32_fp8_e32 v[176:177], v179
	v_cvt_pk_f32_fp8_sdwa v[174:175], v178 src0_sel:WORD_1
	v_cvt_pk_f32_fp8_sdwa v[178:179], v179 src0_sel:WORD_1
	s_waitcnt vmcnt(21)
	v_cvt_pk_f32_fp8_e32 v[188:189], v190
	v_cvt_pk_f32_fp8_sdwa v[190:191], v190 src0_sel:WORD_1
	s_waitcnt vmcnt(17)
	v_cvt_pk_f32_fp8_e32 v[204:205], v206
	v_cvt_pk_f32_fp8_sdwa v[206:207], v206 src0_sel:WORD_1
	v_cvt_pk_f32_fp8_e32 v[192:193], v194
	s_waitcnt vmcnt(13)
	v_cvt_pk_f32_fp8_e32 v[220:221], v222
	v_cvt_pk_f32_fp8_sdwa v[222:223], v222 src0_sel:WORD_1
	v_cvt_pk_f32_fp8_sdwa v[194:195], v194 src0_sel:WORD_1
	v_cvt_pk_f32_fp8_e32 v[208:209], v210
	s_waitcnt vmcnt(9)
	v_cvt_pk_f32_fp8_e32 v[236:237], v238
	v_cvt_pk_f32_fp8_sdwa v[238:239], v238 src0_sel:WORD_1
	v_cvt_pk_f32_fp8_sdwa v[210:211], v210 src0_sel:WORD_1
	v_cvt_pk_f32_fp8_e32 v[224:225], v226
	s_waitcnt vmcnt(5)
	v_cvt_pk_f32_fp8_e32 v[144:145], v244
	v_cvt_pk_f32_fp8_sdwa v[146:147], v244 src0_sel:WORD_1
	v_cvt_pk_f32_fp8_sdwa v[226:227], v226 src0_sel:WORD_1
	v_cvt_pk_f32_fp8_e32 v[240:241], v242
	v_cvt_pk_f32_fp8_sdwa v[242:243], v242 src0_sel:WORD_1
	v_pk_fma_f32 v[172:173], v[172:173], v[94:95], 0 op_sel_hi:[1,0,0]
	v_cvt_pk_f32_fp8_e32 v[150:151], v248
	v_cvt_pk_f32_fp8_sdwa v[148:149], v248 src0_sel:WORD_1
	v_pk_fma_f32 v[156:157], v[160:161], v[92:93], v[156:157] op_sel_hi:[1,0,1]
	s_waitcnt vmcnt(4)
	v_cvt_pk_f32_fp8_e32 v[160:161], v249
	v_cvt_pk_f32_fp8_sdwa v[248:249], v249 src0_sel:WORD_1
	v_cvt_pk_f32_fp8_e32 v[180:181], v182
	v_cvt_pk_f32_fp8_sdwa v[182:183], v182 src0_sel:WORD_1
	v_cvt_pk_f32_fp8_e32 v[196:197], v198
	v_cvt_pk_f32_fp8_sdwa v[198:199], v198 src0_sel:WORD_1
	v_cvt_pk_f32_fp8_e32 v[212:213], v214
	v_cvt_pk_f32_fp8_sdwa v[214:215], v214 src0_sel:WORD_1
	v_cvt_pk_f32_fp8_e32 v[228:229], v230
	v_cvt_pk_f32_fp8_sdwa v[230:231], v230 src0_sel:WORD_1
	v_cvt_pk_f32_fp8_e32 v[244:245], v246
	v_cvt_pk_f32_fp8_sdwa v[246:247], v246 src0_sel:WORD_1
	v_pk_fma_f32 v[158:159], v[162:163], v[92:93], v[158:159] op_sel_hi:[1,0,1]
	s_waitcnt vmcnt(3)
	v_cvt_pk_f32_fp8_e32 v[162:163], v250
	v_pk_fma_f32 v[172:173], v[176:177], v[92:93], v[172:173] op_sel_hi:[1,0,1]
	v_cvt_pk_f32_fp8_sdwa v[176:177], v250 src0_sel:WORD_1
	v_cvt_pk_f32_fp8_e32 v[184:185], v186
	v_cvt_pk_f32_fp8_sdwa v[186:187], v186 src0_sel:WORD_1
	v_pk_fma_f32 v[174:175], v[174:175], v[94:95], 0 op_sel_hi:[1,0,0]
	v_cvt_pk_f32_fp8_e32 v[200:201], v202
	v_cvt_pk_f32_fp8_sdwa v[202:203], v202 src0_sel:WORD_1
	v_cvt_pk_f32_fp8_e32 v[216:217], v218
	v_cvt_pk_f32_fp8_sdwa v[218:219], v218 src0_sel:WORD_1
	v_cvt_pk_f32_fp8_e32 v[232:233], v234
	v_cvt_pk_f32_fp8_sdwa v[234:235], v234 src0_sel:WORD_1
	v_pk_fma_f32 v[190:191], v[190:191], v[94:95], 0 op_sel_hi:[1,0,0]
	v_pk_fma_f32 v[188:189], v[188:189], v[94:95], 0 op_sel_hi:[1,0,0]
	v_pk_fma_f32 v[206:207], v[206:207], v[94:95], 0 op_sel_hi:[1,0,0]
	v_pk_fma_f32 v[204:205], v[204:205], v[94:95], 0 op_sel_hi:[1,0,0]
	v_pk_fma_f32 v[222:223], v[222:223], v[94:95], 0 op_sel_hi:[1,0,0]
	v_pk_fma_f32 v[220:221], v[220:221], v[94:95], 0 op_sel_hi:[1,0,0]
	v_pk_fma_f32 v[238:239], v[238:239], v[94:95], 0 op_sel_hi:[1,0,0]
	v_pk_fma_f32 v[236:237], v[236:237], v[94:95], 0 op_sel_hi:[1,0,0]
	v_pk_fma_f32 v[146:147], v[146:147], v[94:95], 0 op_sel_hi:[1,0,0]
	v_pk_fma_f32 v[144:145], v[144:145], v[94:95], 0 op_sel_hi:[1,0,0]
	v_pk_fma_f32 v[174:175], v[178:179], v[92:93], v[174:175] op_sel_hi:[1,0,1]
	s_waitcnt vmcnt(2)
; #define GAS __attribute__((address_space(1)))
; __global__ void __launch_bounds__(NTHR, 2) mk_fwd(Args args) {
;     ...
;             for (int q = 0; q < 8; ++q) { const int c = 4 * lane + 256 * q; f32x4 f = (f32x4){0.f, 0.f, 0.f, 0.f};
; #pragma unroll
;                 for (int k = 0; k < 4; ++k) { const unsigned yv = *(const GAS unsigned*)(YS + (size_t)sl[k] * D + c); const f32x2n lo2 = __builtin_amdgcn_cvt_pk_f32_fp8(yv, false), hi2 = __builtin_amdgcn_cvt_pk_f32_fp8(yv, true); f += (gt[k] * (1.0f / pg8::YS_SCALE)) * (f32x4){lo2.x, lo2.y, hi2.x, hi2.y}; }
;                 { const v2u hw = *(const GAS v2u*)(H + (size_t)m * D + c); v[q] = ALPHA * (f32x4){bflo(hw.x), bfhi(hw.x), bflo(hw.y), bfhi(hw.y)} + f; } s += (v[q].x + v[q].y) + (v[q].z + v[q].w); }
	v_cvt_pk_f32_fp8_e32 v[178:179], v251
	v_cvt_pk_f32_fp8_sdwa v[250:251], v251 src0_sel:WORD_1
	v_pk_fma_f32 v[188:189], v[192:193], v[92:93], v[188:189] op_sel_hi:[1,0,1]
	v_pk_fma_f32 v[190:191], v[194:195], v[92:93], v[190:191] op_sel_hi:[1,0,1]
	v_pk_fma_f32 v[192:193], v[208:209], v[92:93], v[204:205] op_sel_hi:[1,0,1]
	v_pk_fma_f32 v[194:195], v[210:211], v[92:93], v[206:207] op_sel_hi:[1,0,1]
	v_pk_fma_f32 v[204:205], v[224:225], v[92:93], v[220:221] op_sel_hi:[1,0,1]
	v_pk_fma_f32 v[206:207], v[226:227], v[92:93], v[222:223] op_sel_hi:[1,0,1]
	v_pk_fma_f32 v[208:209], v[240:241], v[92:93], v[236:237] op_sel_hi:[1,0,1]
	v_pk_fma_f32 v[210:211], v[242:243], v[92:93], v[238:239] op_sel_hi:[1,0,1]
	v_pk_fma_f32 v[144:145], v[160:161], v[92:93], v[144:145] op_sel_hi:[1,0,1]
	v_pk_fma_f32 v[146:147], v[248:249], v[92:93], v[146:147] op_sel_hi:[1,0,1]
	v_pk_fma_f32 v[152:153], v[152:153], v[68:69], v[66:67] op_sel_hi:[1,0,1]
	v_pk_fma_f32 v[142:143], v[154:155], v[68:69], v[142:143] op_sel_hi:[1,0,1]
	v_pk_fma_f32 v[154:155], v[166:167], v[64:65], v[158:159] op_sel_hi:[1,0,1]
	v_pk_fma_f32 v[156:157], v[164:165], v[64:65], v[156:157] op_sel_hi:[1,0,1]
	v_pk_fma_f32 v[158:159], v[182:183], v[64:65], v[174:175] op_sel_hi:[1,0,1]
	v_pk_fma_f32 v[160:161], v[180:181], v[64:65], v[172:173] op_sel_hi:[1,0,1]
	v_pk_fma_f32 v[164:165], v[198:199], v[64:65], v[190:191] op_sel_hi:[1,0,1]
	v_pk_fma_f32 v[166:167], v[196:197], v[64:65], v[188:189] op_sel_hi:[1,0,1]
	v_pk_fma_f32 v[172:173], v[214:215], v[64:65], v[194:195] op_sel_hi:[1,0,1]
	v_pk_fma_f32 v[174:175], v[212:213], v[64:65], v[192:193] op_sel_hi:[1,0,1]
	v_pk_fma_f32 v[180:181], v[230:231], v[64:65], v[206:207] op_sel_hi:[1,0,1]
	v_pk_fma_f32 v[182:183], v[228:229], v[64:65], v[204:205] op_sel_hi:[1,0,1]
	v_pk_fma_f32 v[188:189], v[246:247], v[64:65], v[210:211] op_sel_hi:[1,0,1]
	v_pk_fma_f32 v[190:191], v[244:245], v[64:65], v[208:209] op_sel_hi:[1,0,1]
	v_pk_fma_f32 v[146:147], v[176:177], v[64:65], v[146:147] op_sel_hi:[1,0,1]
	v_pk_fma_f32 v[144:145], v[162:163], v[64:65], v[144:145] op_sel_hi:[1,0,1]
	s_waitcnt vmcnt(1)
	v_mov_b64_e32 v[66:67], v[98:99]
	v_mov_b64_e32 v[64:65], v[96:97]
	v_pk_fma_f32 v[96:97], v[126:127], s[12:13], v[142:143] op_sel_hi:[1,0,1]
	v_pk_fma_f32 v[98:99], v[124:125], s[12:13], v[152:153] op_sel_hi:[1,0,1]
	v_pk_fma_f32 v[124:125], v[168:169], v[68:69], v[156:157] op_sel_hi:[1,0,1]
	v_pk_fma_f32 v[126:127], v[170:171], v[68:69], v[154:155] op_sel_hi:[1,0,1]
	v_lshlrev_b32_e32 v130, 16, v104
	v_and_b32_e32 v131, 0xffff0000, v104
	v_lshlrev_b32_e32 v104, 16, v105
	v_and_b32_e32 v105, 0xffff0000, v105
	v_pk_fma_f32 v[142:143], v[184:185], v[68:69], v[160:161] op_sel_hi:[1,0,1]
	v_pk_fma_f32 v[152:153], v[186:187], v[68:69], v[158:159] op_sel_hi:[1,0,1]
	v_pk_fma_f32 v[126:127], v[70:71], s[12:13], v[126:127] op_sel_hi:[1,0,1]
	v_pk_fma_f32 v[124:125], v[128:129], s[12:13], v[124:125] op_sel_hi:[1,0,1]
	v_lshlrev_b32_e32 v140, 16, v116
	v_and_b32_e32 v141, 0xffff0000, v116
	v_lshlrev_b32_e32 v116, 16, v117
	v_and_b32_e32 v117, 0xffff0000, v117
	v_pk_fma_f32 v[154:155], v[200:201], v[68:69], v[166:167] op_sel_hi:[1,0,1]
	v_pk_fma_f32 v[156:157], v[202:203], v[68:69], v[164:165] op_sel_hi:[1,0,1]
	v_pk_fma_f32 v[158:159], v[216:217], v[68:69], v[174:175] op_sel_hi:[1,0,1]
	v_pk_fma_f32 v[160:161], v[218:219], v[68:69], v[172:173] op_sel_hi:[1,0,1]
	v_pk_fma_f32 v[162:163], v[232:233], v[68:69], v[182:183] op_sel_hi:[1,0,1]
	v_pk_fma_f32 v[164:165], v[234:235], v[68:69], v[180:181] op_sel_hi:[1,0,1]
	v_pk_fma_f32 v[150:151], v[150:151], v[68:69], v[190:191] op_sel_hi:[1,0,1]
	v_pk_fma_f32 v[148:149], v[148:149], v[68:69], v[188:189] op_sel_hi:[1,0,1]
	v_pk_fma_f32 v[144:145], v[178:179], v[68:69], v[144:145] op_sel_hi:[1,0,1]
	v_pk_fma_f32 v[68:69], v[250:251], v[68:69], v[146:147] op_sel_hi:[1,0,1]
	v_mov_b32_e32 v128, v98
	v_mov_b32_e32 v146, v99
	v_mov_b32_e32 v166, v96
	v_mov_b32_e32 v168, v97
	v_pk_fma_f32 v[104:105], v[104:105], s[12:13], v[152:153] op_sel_hi:[1,0,1]
	v_pk_fma_f32 v[130:131], v[130:131], s[12:13], v[142:143] op_sel_hi:[1,0,1]
	v_mov_b32_e32 v129, v124
	v_mov_b32_e32 v147, v125
	v_mov_b32_e32 v167, v126
	v_mov_b32_e32 v169, v127
	v_pk_fma_f32 v[116:117], v[116:117], s[12:13], v[68:69] op_sel_hi:[1,0,1]
	s_waitcnt vmcnt(0)
; #define GAS __attribute__((address_space(1)))
; __device__ __forceinline__ float wave_sum_dpp(float x) {
;     x = row16_sum(x);
;     x += __builtin_bit_cast(float, __builtin_amdgcn_update_dpp(0, __builtin_bit_cast(int, x), 0x142, 0xA, 0xF, false));
;     x += __builtin_bit_cast(float, __builtin_amdgcn_update_dpp(0, __builtin_bit_cast(int, x), 0x143, 0xC, 0xF, false));
;     return __builtin_bit_cast(float, __builtin_amdgcn_readlane(__builtin_bit_cast(int, x), 63));
; __global__ void __launch_bounds__(NTHR, 2) mk_fwd(Args args) {
;     ...
;                 { const v2u hw = *(const GAS v2u*)(H + (size_t)m * D + c); v[q] = ALPHA * (f32x4){bflo(hw.x), bfhi(hw.x), bflo(hw.y), bfhi(hw.y)} + f; } s += (v[q].x + v[q].y) + (v[q].z + v[q].w); }
;             const float mean = wave_sum_dpp(s) * (1.0f / D); float s2 = 0.f;
; #pragma unroll
;             for (int q = 0; q < 8; ++q) { v[q] = v[q] - mean; s2 += (v[q].x * v[q].x + v[q].y * v[q].y) + (v[q].z * v[q].z + v[q].w * v[q].w); }
	v_mov_b64_e32 v[70:71], v[102:103]
	v_mov_b64_e32 v[68:69], v[100:101]
	v_pk_mov_b32 v[100:101], v[130:131], v[104:105] op_sel:[1,0]
	v_mov_b32_e32 v102, v130
	v_mov_b32_e32 v103, v105
	v_pk_add_f32 v[128:129], v[128:129], v[146:147]
	v_pk_add_f32 v[146:147], v[166:167], v[168:169]
	v_lshlrev_b32_e32 v132, 16, v108
	v_and_b32_e32 v133, 0xffff0000, v108
	v_lshlrev_b32_e32 v108, 16, v109
	v_and_b32_e32 v109, 0xffff0000, v109
	v_lshlrev_b32_e32 v134, 16, v110
	v_and_b32_e32 v135, 0xffff0000, v110
	v_lshlrev_b32_e32 v110, 16, v111
	v_and_b32_e32 v111, 0xffff0000, v111
	v_pk_add_f32 v[100:101], v[100:101], v[102:103]
	v_pk_add_f32 v[128:129], v[128:129], v[146:147]
	v_lshlrev_b32_e32 v136, 16, v112
	v_and_b32_e32 v137, 0xffff0000, v112
	v_lshlrev_b32_e32 v112, 16, v113
	v_and_b32_e32 v113, 0xffff0000, v113
	v_lshlrev_b32_e32 v138, 16, v114
	v_and_b32_e32 v139, 0xffff0000, v114
	v_lshlrev_b32_e32 v114, 16, v115
	v_and_b32_e32 v115, 0xffff0000, v115
	v_pk_fma_f32 v[108:109], v[108:109], s[12:13], v[156:157] op_sel_hi:[1,0,1]
	v_pk_fma_f32 v[132:133], v[132:133], s[12:13], v[154:155] op_sel_hi:[1,0,1]
	v_pk_fma_f32 v[110:111], v[110:111], s[12:13], v[160:161] op_sel_hi:[1,0,1]
	v_pk_fma_f32 v[134:135], v[134:135], s[12:13], v[158:159] op_sel_hi:[1,0,1]
	v_pk_add_f32 v[100:101], v[100:101], v[100:101] op_sel:[0,1] op_sel_hi:[1,0]
	v_add_f32_e32 v92, 0, v128
	v_pk_fma_f32 v[112:113], v[112:113], s[12:13], v[164:165] op_sel_hi:[1,0,1]
	v_pk_fma_f32 v[136:137], v[136:137], s[12:13], v[162:163] op_sel_hi:[1,0,1]
	v_pk_fma_f32 v[114:115], v[114:115], s[12:13], v[148:149] op_sel_hi:[1,0,1]
	v_pk_fma_f32 v[140:141], v[140:141], s[12:13], v[144:145] op_sel_hi:[1,0,1]
	v_add_f32_e32 v142, v132, v133
	v_add_f32_e32 v144, v108, v109
	v_mov_b32_e32 v149, v134
	v_mov_b32_e32 v143, v110
	v_mov_b32_e32 v145, v111
	v_mov_b32_e32 v101, v135
	v_add_f32_e32 v148, v92, v129
	v_pk_fma_f32 v[138:139], v[138:139], s[12:13], v[150:151] op_sel_hi:[1,0,1]
	v_pk_mov_b32 v[150:151], v[136:137], v[112:113] op_sel:[1,0]
	v_mov_b32_e32 v152, v136
	v_mov_b32_e32 v153, v113
	v_pk_add_f32 v[102:103], v[142:143], v[144:145]
	v_pk_add_f32 v[100:101], v[148:149], v[100:101]
	v_pk_add_f32 v[142:143], v[150:151], v[152:153]
	v_pk_add_f32 v[100:101], v[100:101], v[102:103]
	v_pk_add_f32 v[142:143], v[142:143], v[142:143] op_sel:[0,1] op_sel_hi:[1,0]
	v_pk_add_f32 v[100:101], v[100:101], v[100:101] op_sel:[0,1] op_sel_hi:[1,0]
	v_add_f32_e32 v154, v138, v139
	v_add_f32_e32 v156, v114, v115
	v_mov_b32_e32 v155, v116
	v_mov_b32_e32 v157, v117
	v_mov_b32_e32 v143, v141
	v_mov_b32_e32 v101, v140
	v_pk_add_f32 v[144:145], v[154:155], v[156:157]
	v_pk_add_f32 v[100:101], v[100:101], v[142:143]
	s_nop 0
	v_pk_add_f32 v[100:101], v[100:101], v[144:145]
	s_nop 0
	v_add_f32_e32 v92, v100, v101
	s_nop 1
	v_add_f32_dpp v92, v92, v92 quad_perm:[1,0,3,2] row_mask:0xf bank_mask:0xf bound_ctrl:1
	s_nop 1
	v_add_f32_dpp v92, v92, v92 quad_perm:[2,3,0,1] row_mask:0xf bank_mask:0xf bound_ctrl:1
	s_nop 1
	v_add_f32_dpp v92, v92, v92 row_half_mirror row_mask:0xf bank_mask:0xf bound_ctrl:1
	s_nop 1
	v_add_f32_dpp v92, v92, v92 row_mirror row_mask:0xf bank_mask:0xf bound_ctrl:1
	s_nop 1
	v_mov_b32_dpp v120, v92 row_bcast:15 row_mask:0xa bank_mask:0xf
	v_add_f32_e32 v92, v92, v120
	s_nop 1
	v_mov_b32_dpp v121, v92 row_bcast:31 row_mask:0xc bank_mask:0xf
	v_add_f32_e32 v92, v92, v121
	s_nop 0
	v_readlane_b32 s2, v92, 63
	s_nop 1
	v_fmac_f32_e32 v97, s2, v118
	v_fmac_f32_e32 v99, s2, v118
	v_fmac_f32_e32 v127, s2, v118
	v_fmac_f32_e32 v125, s2, v118
	v_fma_f32 v96, s2, v118, v96
	v_fma_f32 v98, s2, v118, v98
	v_fma_f32 v126, s2, v118, v126
	v_fma_f32 v124, s2, v118, v124
	v_fmac_f32_e32 v105, s2, v118
	v_fmac_f32_e32 v131, s2, v118
	v_mul_f32_e32 v92, v99, v99
	v_mul_f32_e32 v94, v97, v97
	v_mul_f32_e32 v100, v125, v125
	v_mul_f32_e32 v101, v127, v127
	v_fma_f32 v104, s2, v118, v104
	v_fma_f32 v130, s2, v118, v130
	v_fmac_f32_e32 v109, s2, v118
	v_fmac_f32_e32 v133, s2, v118
	v_mul_f32_e32 v102, v131, v131
	v_mul_f32_e32 v103, v105, v105
	v_fmac_f32_e32 v92, v98, v98
	v_fmac_f32_e32 v94, v96, v96
	v_fmac_f32_e32 v100, v124, v124
	v_fmac_f32_e32 v101, v126, v126
	v_fma_f32 v108, s2, v118, v108
	v_fma_f32 v132, s2, v118, v132
	v_fmac_f32_e32 v111, s2, v118
	v_fmac_f32_e32 v135, s2, v118
	v_mul_f32_e32 v120, v133, v133
	v_mul_f32_e32 v121, v109, v109
	v_fmac_f32_e32 v102, v130, v130
	v_fmac_f32_e32 v103, v104, v104
	v_add_f32_e32 v92, v92, v94
	v_add_f32_e32 v94, v100, v101
	v_fma_f32 v110, s2, v118, v110
	v_fma_f32 v134, s2, v118, v134
	v_fmac_f32_e32 v113, s2, v118
	v_fmac_f32_e32 v137, s2, v118
	v_mul_f32_e32 v128, v135, v135
	v_mul_f32_e32 v129, v111, v111
	v_fmac_f32_e32 v120, v132, v132
	v_fmac_f32_e32 v121, v108, v108
	v_add_f32_e32 v100, v102, v103
	v_add_f32_e32 v92, v92, v94
	v_fma_f32 v112, s2, v118, v112
	v_fma_f32 v136, s2, v118, v136
	v_fmac_f32_e32 v115, s2, v118
	v_fmac_f32_e32 v139, s2, v118
	v_mul_f32_e32 v142, v137, v137
	v_mul_f32_e32 v143, v113, v113
	v_fmac_f32_e32 v128, v134, v134
	v_fmac_f32_e32 v129, v110, v110
	v_add_f32_e32 v101, v120, v121
	v_add_f32_e32 v92, v92, v100
; #define GAS __attribute__((address_space(1)))
; #define LAS __attribute__((address_space(3)))
; __global__ void __launch_bounds__(NTHR, 2) mk_fwd(Args args) {
;     ...
;             const float mean = wave_sum_dpp(s) * (1.0f / D); float s2 = 0.f;
; #pragma unroll
;             for (int q = 0; q < 8; ++q) { v[q] = v[q] - mean; s2 += (v[q].x * v[q].x + v[q].y * v[q].y) + (v[q].z * v[q].z + v[q].w * v[q].w); }
;             const float rstd = 1.0f / sqrtf(wave_sum_dpp(s2) * (1.0f / D) + LN_EPS);
; #pragma unroll
;             for (int q = 0; q < 8; ++q) { const int c = 4 * lane + 256 * q; *(GAS f32x4*)(out + (size_t)m * D + c) = v[q] * rstd * *(const LAS f32x4*)(s_lnw + c) + *(const LAS f32x4*)(s_lnb + c); }
	v_fma_f32 v114, s2, v118, v114
	v_fma_f32 v138, s2, v118, v138
	v_fmac_f32_e32 v117, s2, v118
	v_fmac_f32_e32 v141, s2, v118
	v_mul_f32_e32 v144, v139, v139
	v_mul_f32_e32 v145, v115, v115
	v_fmac_f32_e32 v142, v136, v136
	v_fmac_f32_e32 v143, v112, v112
	v_add_f32_e32 v102, v128, v129
	v_add_f32_e32 v92, v92, v101
	v_fma_f32 v116, s2, v118, v116
	v_fma_f32 v140, s2, v118, v140
	v_mul_f32_e32 v146, v141, v141
	v_mul_f32_e32 v147, v117, v117
	v_fmac_f32_e32 v144, v138, v138
	v_fmac_f32_e32 v145, v114, v114
	v_add_f32_e32 v103, v142, v143
	v_add_f32_e32 v92, v92, v102
	v_fmac_f32_e32 v146, v140, v140
	v_fmac_f32_e32 v147, v116, v116
	v_add_f32_e32 v120, v144, v145
	v_add_f32_e32 v92, v92, v103
	v_add_f32_e32 v121, v146, v147
	v_add_f32_e32 v92, v92, v120
	v_add_f32_e32 v92, v92, v121
	s_nop 1
	v_add_f32_dpp v92, v92, v92 quad_perm:[1,0,3,2] row_mask:0xf bank_mask:0xf bound_ctrl:1
	s_nop 1
	v_add_f32_dpp v92, v92, v92 quad_perm:[2,3,0,1] row_mask:0xf bank_mask:0xf bound_ctrl:1
	s_nop 1
	v_add_f32_dpp v92, v92, v92 row_half_mirror row_mask:0xf bank_mask:0xf bound_ctrl:1
	s_nop 1
	v_add_f32_dpp v92, v92, v92 row_mirror row_mask:0xf bank_mask:0xf bound_ctrl:1
	s_nop 1
	v_mov_b32_dpp v122, v92 row_bcast:15 row_mask:0xa bank_mask:0xf
	v_add_f32_e32 v92, v92, v122
	s_nop 1
	v_mov_b32_dpp v123, v92 row_bcast:31 row_mask:0xc bank_mask:0xf
	v_add_f32_e32 v92, v92, v123
	s_nop 0
	v_readlane_b32 s2, v92, 63
	s_nop 1
	v_fma_f32 v92, s2, v119, v93
	v_mul_f32_e32 v94, 0x4f800000, v92
	v_cmp_gt_f32_e32 vcc, s13, v92
	s_nop 1
	v_cndmask_b32_e32 v92, v92, v94, vcc
	v_sqrt_f32_e32 v94, v92
	s_nop 0
	v_add_u32_e32 v100, -1, v94
	v_add_u32_e32 v101, 1, v94
	v_fma_f32 v102, -v100, v94, v92
	v_fma_f32 v103, -v101, v94, v92
	v_cmp_ge_f32_e64 s[2:3], 0, v102
	s_nop 1
	v_cndmask_b32_e64 v94, v94, v100, s[2:3]
	v_cmp_lt_f32_e64 s[2:3], 0, v103
	s_nop 1
	v_cndmask_b32_e64 v94, v94, v101, s[2:3]
	v_mul_f32_e32 v100, 0x37800000, v94
	v_cndmask_b32_e32 v94, v94, v100, vcc
	v_cmp_class_f32_e32 vcc, v92, v95
	s_nop 1
	v_cndmask_b32_e32 v92, v94, v92, vcc
	v_div_scale_f32 v94, s[2:3], v92, v92, 1.0
	v_rcp_f32_e32 v101, v94
	v_div_scale_f32 v100, vcc, 1.0, v92, 1.0
	v_fma_f32 v102, -v94, v101, 1.0
	v_fmac_f32_e32 v101, v102, v101
	v_mul_f32_e32 v102, v100, v101
	v_fma_f32 v103, -v94, v102, v100
	v_fmac_f32_e32 v102, v103, v101
	v_fma_f32 v94, -v94, v102, v100
	v_div_fmas_f32 v94, v94, v101, v102
	v_div_fixup_f32 v92, v94, v92, 1.0
	v_pk_mul_f32 v[100:101], v[92:93], v[98:99] op_sel_hi:[0,1]
	v_pk_mul_f32 v[96:97], v[92:93], v[96:97] op_sel_hi:[0,1]
	v_pk_mul_f32 v[120:121], v[92:93], v[124:125] op_sel_hi:[0,1]
	v_pk_mul_f32 v[102:103], v[92:93], v[126:127] op_sel_hi:[0,1]
	v_pk_mul_f32 v[122:123], v[92:93], v[130:131] op_sel_hi:[0,1]
	v_pk_mul_f32 v[104:105], v[92:93], v[104:105] op_sel_hi:[0,1]
	v_pk_mul_f32 v[124:125], v[92:93], v[132:133] op_sel_hi:[0,1]
	v_pk_mul_f32 v[126:127], v[92:93], v[108:109] op_sel_hi:[0,1]
	v_pk_mul_f32 v[128:129], v[92:93], v[134:135] op_sel_hi:[0,1]
	v_pk_mul_f32 v[130:131], v[92:93], v[110:111] op_sel_hi:[0,1]
	v_pk_mul_f32 v[132:133], v[92:93], v[136:137] op_sel_hi:[0,1]
	v_pk_mul_f32 v[134:135], v[92:93], v[112:113] op_sel_hi:[0,1]
	v_pk_mul_f32 v[136:137], v[92:93], v[138:139] op_sel_hi:[0,1]
	v_pk_mul_f32 v[138:139], v[92:93], v[114:115] op_sel_hi:[0,1]
	v_pk_mul_f32 v[140:141], v[92:93], v[140:141] op_sel_hi:[0,1]
	v_pk_mul_f32 v[116:117], v[92:93], v[116:117] op_sel_hi:[0,1]
	s_waitcnt lgkmcnt(13)
	v_pk_fma_f32 v[98:99], v[96:97], v[2:3], v[10:11]
	v_pk_fma_f32 v[96:97], v[100:101], v[0:1], v[8:9]
	s_waitcnt lgkmcnt(12)
	v_pk_fma_f32 v[102:103], v[102:103], v[6:7], v[14:15]
	v_pk_fma_f32 v[100:101], v[120:121], v[4:5], v[12:13]
	s_waitcnt lgkmcnt(9)
	v_pk_fma_f32 v[110:111], v[104:105], v[18:19], v[26:27]
	v_pk_fma_f32 v[108:109], v[122:123], v[16:17], v[24:25]
	s_waitcnt lgkmcnt(8)
	v_pk_fma_f32 v[114:115], v[126:127], v[22:23], v[30:31]
	v_pk_fma_f32 v[112:113], v[124:125], v[20:21], v[28:29]
	s_waitcnt lgkmcnt(5)
	v_pk_fma_f32 v[122:123], v[130:131], v[34:35], v[42:43]
	v_pk_fma_f32 v[120:121], v[128:129], v[32:33], v[40:41]
	s_waitcnt lgkmcnt(4)
	v_pk_fma_f32 v[126:127], v[134:135], v[38:39], v[46:47]
	v_pk_fma_f32 v[124:125], v[132:133], v[36:37], v[44:45]
	s_waitcnt lgkmcnt(1)
	v_pk_fma_f32 v[130:131], v[138:139], v[50:51], v[58:59]
	v_pk_fma_f32 v[128:129], v[136:137], v[48:49], v[56:57]
	s_waitcnt lgkmcnt(0)
	v_pk_fma_f32 v[134:135], v[116:117], v[54:55], v[62:63]
	v_pk_fma_f32 v[132:133], v[140:141], v[52:53], v[60:61]
	global_store_dwordx4 v[106:107], v[96:99], off offset:-3072 nt
	global_store_dwordx4 v[106:107], v[100:103], off offset:-2048 nt
	global_store_dwordx4 v[106:107], v[108:111], off offset:-1024 nt
	global_store_dwordx4 v[88:89], v[112:115], off offset:-4096 nt
	global_store_dwordx4 v[88:89], v[120:123], off offset:-3072 nt
	global_store_dwordx4 v[88:89], v[124:127], off offset:-2048 nt
	global_store_dwordx4 v[88:89], v[128:131], off offset:-1024 nt
	global_store_dwordx4 v[88:89], v[132:135], off nt
	v_lshl_add_u64 v[88:89], v[88:89], 0, s[6:7]
	s_mov_b64 vcc, s[0:1]
	s_cbranch_vccnz .LBB0_1219
